# speedup vs baseline: 1.0990x; 1.0380x over previous
.LBB0_9:
	s_or_b64 exec, exec, s[8:9]
	s_mul_i32 s3, s2, 0xc35
	v_add_u32_e32 v2, s3, v0
	v_mov_b32_e32 v3, 0
	v_lshlrev_b64 v[4:5], 2, v[2:3]
	s_waitcnt lgkmcnt(0)
	v_lshl_add_u64 v[6:7], s[6:7], 0, v[4:5]
	v_lshl_add_u64 v[4:5], s[4:5], 0, v[4:5]
	s_barrier
	global_load_dword v10, v[4:5], off
	v_add_u32_e32 v4, 0x400, v2
	v_mov_b32_e32 v5, v3
	v_lshlrev_b64 v[4:5], 2, v[4:5]
	global_load_dword v9, v[6:7], off
	v_lshl_add_u64 v[6:7], s[6:7], 0, v[4:5]
	v_lshl_add_u64 v[4:5], s[4:5], 0, v[4:5]
	global_load_dword v12, v[4:5], off
	v_add_u32_e32 v4, 0x800, v2
	v_mov_b32_e32 v5, v3
	v_lshlrev_b64 v[4:5], 2, v[4:5]
	global_load_dword v11, v[6:7], off
	v_lshl_add_u64 v[6:7], s[6:7], 0, v[4:5]
	v_lshl_add_u64 v[4:5], s[4:5], 0, v[4:5]
	global_load_dword v13, v[6:7], off
	s_movk_i32 s8, 0xc35
	global_load_dword v4, v[4:5], off
	v_or_b32_e32 v8, 0xc00, v0
	v_cmp_gt_u32_e32 vcc, s8, v8
	s_and_saveexec_b64 s[8:9], vcc
	s_cbranch_execz .Lkp_skip
	v_add_u32_e32 v14, s3, v8
	v_mov_b32_e32 v15, 0
	v_lshlrev_b64 v[14:15], 2, v[14:15]
	v_lshl_add_u64 v[16:17], s[6:7], 0, v[14:15]
	v_lshl_add_u64 v[14:15], s[4:5], 0, v[14:15]
	global_load_dword v16, v[16:17], off
	global_load_dword v17, v[14:15], off
.Lkp_skip:
	s_or_b64 exec, exec, s[8:9]
	s_waitcnt vmcnt(4)
	v_lshl_or_b32 v7, v9, 16, v10
	s_waitcnt vmcnt(2)
	v_lshl_or_b32 v6, v11, 16, v12
	s_waitcnt vmcnt(0)
	v_lshl_or_b32 v5, v13, 16, v4
	v_mov_b32_e32 v4, v3
	s_and_saveexec_b64 s[8:9], vcc
	s_cbranch_execz .LBB0_11
	v_lshl_or_b32 v4, v16, 16, v17

_Z5k_degPKjPKhS0_S0_P15HIP_vector_typeIiLj2EEPi:
	s_load_dwordx4 s[8:11], s[0:1], 0x10
	s_movk_i32 s3, 0xff
	v_cmp_lt_u32_e64 s[4:5], s3, v0
	s_movk_i32 s3, 0x100
	v_cmp_gt_u32_e64 s[38:39], s3, v0
	v_lshlrev_b32_e32 v1, 2, v0
	s_and_saveexec_b64 s[6:7], s[38:39]
	v_mov_b32_e32 v2, 0
	ds_write_b32 v1, v2 offset:2048
	s_or_b64 exec, exec, s[6:7]
	v_cmp_eq_u32_e32 vcc, 0, v0
	s_and_saveexec_b64 s[6:7], vcc
	v_mov_b32_e32 v2, 0
	ds_write_b32 v2, v2 offset:3072
	s_or_b64 exec, exec, s[6:7]
	s_waitcnt lgkmcnt(0)
	v_mov_b32_e32 v3, s9
	v_mov_b32_e32 v4, s11
	v_cndmask_b32_e64 v5, v3, v4, s[4:5]
	v_mov_b32_e32 v3, s8
	v_mov_b32_e32 v4, s10
	v_and_b32_e32 v2, 0xff, v0
	v_cndmask_b32_e64 v4, v3, v4, s[4:5]
	s_movk_i32 s3, 0x187
	v_mov_b32_e32 v3, s2
	v_mad_u32_u24 v6, v2, s3, v3
	v_ashrrev_i32_e32 v7, 31, v6
	v_lshl_add_u64 v[4:5], v[6:7], 2, v[4:5]
	global_load_dword v4, v[4:5], off
	s_load_dwordx4 s[60:63], s[0:1], 0x0
	s_load_dwordx4 s[56:59], s[0:1], 0x20
	v_lshrrev_b32_e32 v8, 8, v0
	s_mov_b32 s0, 0xffff
	s_xor_b64 s[4:5], s[4:5], -1
	v_lshlrev_b32_e32 v3, 10, v8
	v_lshl_or_b32 v5, v2, 2, v3
	s_waitcnt vmcnt(0)
	v_cmp_lt_u32_e64 s[0:1], s0, v4
	s_and_b64 s[0:1], s[4:5], s[0:1]
	ds_write_b32 v5, v4
	s_waitcnt lgkmcnt(0)
	s_barrier
	v_lshrrev_b32_e32 v4, 16, v4
	s_nop 0
	v_cndmask_b32_e64 v4, 0, v4, s[0:1]
	s_nop 1
	v_add_u32_dpp v4, v4, v4 quad_perm:[1,0,3,2] row_mask:0xf bank_mask:0xf
	s_nop 1
	v_add_u32_dpp v4, v4, v4 quad_perm:[2,3,0,1] row_mask:0xf bank_mask:0xf
	s_nop 1
	v_add_u32_dpp v4, v4, v4 row_half_mirror row_mask:0xf bank_mask:0xf
	s_nop 1
	v_add_u32_dpp v4, v4, v4 row_mirror row_mask:0xf bank_mask:0xf
	s_nop 1
	v_add_u32_dpp v4, v4, v4 row_bcast:15 row_mask:0xa bank_mask:0xf
	s_nop 1
	v_add_u32_dpp v4, v4, v4 row_bcast:31 row_mask:0xc bank_mask:0xf
	s_nop 1
	v_readlane_b32 s3, v4, 63
	s_mov_b64 s[4:5], exec
	s_cmp_eq_u32 s3, 0
	s_cbranch_scc1 .LBB1_9
	v_mov_b32_e32 v4, 0
	v_mov_b32_e32 v5, s3
	s_mov_b64 exec, 1
	ds_add_u32 v4, v5 offset:3072

_Z5k_csrPKjS0_PK15HIP_vector_typeIiLj2EEPKiPiPjPS1_IfLj2EE:
	s_load_dwordx2 s[6:7], s[0:1], 0x18
	s_load_dwordx4 s[56:59], s[0:1], 0x8
	v_cmp_gt_i32_e32 vcc, s2, v0
	v_or_b32_e32 v2, 0x100, v0
	v_cmp_gt_i32_e64 s[4:5], s2, v2
	v_cndmask_b32_e32 v1, 0, v0, vcc
	v_lshlrev_b32_e32 v1, 2, v1
	v_cndmask_b32_e64 v2, 0, v2, s[4:5]
	v_lshlrev_b32_e32 v2, 2, v2
	s_waitcnt lgkmcnt(0)
	global_load_dword v3, v1, s[6:7]
	global_load_dword v4, v2, s[6:7]
	s_movk_i32 s3, 0x187
	v_mov_b32_e32 v122, s2
	v_mad_u32_u24 v122, v0, s3, v122
	v_ashrrev_i32_e32 v123, 31, v122
	v_lshl_add_u64 v[122:123], v[122:123], 2, s[56:57]
	global_load_dword v125, v[122:123], off
	v_lshl_add_u32 v122, s2, 7, v0
	v_mov_b32_e32 v124, 0
	s_movk_i32 s3, 0x80
	v_cmp_gt_u32_e64 s[8:9], s3, v0
	s_mov_b32 s3, 0xc350
	v_cmp_gt_i32_e64 s[10:11], s3, v122
	v_ashrrev_i32_e32 v123, 31, v122
	s_and_b64 s[8:9], s[8:9], s[10:11]
	s_and_saveexec_b64 s[10:11], s[8:9]
	v_lshl_add_u64 v[122:123], v[122:123], 3, s[58:59]
	global_load_dword v124, v[122:123], off
	s_or_b64 exec, exec, s[10:11]
	v_mbcnt_lo_u32_b32 v1, -1, 0
	v_mbcnt_hi_u32_b32 v10, -1, v1
	v_and_b32_e32 v11, 64, v10
	v_xor_b32_e32 v1, 32, v10
	v_add_u32_e32 v2, 64, v11
	v_cmp_lt_i32_e64 s[6:7], v1, v2
	v_and_b32_e32 v24, 63, v0
	v_lshrrev_b32_e32 v8, 6, v0
	v_cndmask_b32_e64 v1, v10, v1, s[6:7]
	v_lshlrev_b32_e32 v1, 2, v1
	v_cmp_eq_u32_e64 s[6:7], 0, v24
	v_lshlrev_b32_e32 v13, 2, v8
	s_waitcnt vmcnt(2)
	v_cndmask_b32_e32 v3, 0, v3, vcc
	s_waitcnt vmcnt(1)
	v_cndmask_b32_e64 v4, 0, v4, s[4:5]
	v_add_u32_e32 v3, v4, v3
	ds_bpermute_b32 v1, v1, v3
	v_xor_b32_e32 v4, 16, v10
	v_cmp_lt_i32_e32 vcc, v4, v2
	s_waitcnt lgkmcnt(0)
	v_add_u32_e32 v1, v1, v3
	v_cndmask_b32_e32 v4, v10, v4, vcc
	v_lshlrev_b32_e32 v4, 2, v4
	ds_bpermute_b32 v3, v4, v1
	v_xor_b32_e32 v4, 8, v10
	v_cmp_lt_i32_e32 vcc, v4, v2
	s_waitcnt lgkmcnt(0)
	v_add_u32_e32 v1, v3, v1
	v_cndmask_b32_e32 v4, v10, v4, vcc
	v_lshlrev_b32_e32 v4, 2, v4
	ds_bpermute_b32 v3, v4, v1
	v_xor_b32_e32 v4, 4, v10
	v_cmp_lt_i32_e32 vcc, v4, v2
	s_waitcnt lgkmcnt(0)
	v_add_u32_e32 v1, v3, v1
	v_cndmask_b32_e32 v4, v10, v4, vcc
	v_lshlrev_b32_e32 v4, 2, v4
	ds_bpermute_b32 v3, v4, v1
	v_xor_b32_e32 v4, 2, v10
	v_cmp_lt_i32_e32 vcc, v4, v2
	s_waitcnt lgkmcnt(0)
	v_add_u32_e32 v1, v3, v1
	v_cndmask_b32_e32 v4, v10, v4, vcc
	v_lshlrev_b32_e32 v4, 2, v4
	ds_bpermute_b32 v3, v4, v1
	v_xor_b32_e32 v4, 1, v10
	v_cmp_lt_i32_e32 vcc, v4, v2
	s_waitcnt lgkmcnt(0)
	v_add_u32_e32 v1, v3, v1
	v_cndmask_b32_e32 v2, v10, v4, vcc
	v_lshlrev_b32_e32 v2, 2, v2
	ds_bpermute_b32 v2, v2, v1
	s_and_saveexec_b64 s[4:5], s[6:7]
	s_cbranch_execz .LBB2_2
	s_waitcnt lgkmcnt(0)
	v_add_u32_e32 v1, v2, v1
	ds_write_b32 v13, v1 offset:4096
.LBB2_2:
	s_or_b64 exec, exec, s[4:5]
	s_movk_i32 s3, 0x187
	v_mov_b32_e32 v1, s2
	s_waitcnt lgkmcnt(0)
	v_mad_u32_u24 v2, v0, s3, v1
	v_ashrrev_i32_e32 v3, 31, v2
	v_lshl_add_u64 v[2:3], v[2:3], 2, s[56:57]
	s_nop 0
	s_load_dwordx2 s[60:61], s[0:1], 0x0
	s_load_dwordx4 s[52:55], s[0:1], 0x20
	s_load_dwordx2 s[56:57], s[0:1], 0x30
	s_movk_i32 s0, 0x80
	v_lshlrev_b32_e32 v1, 2, v0
	v_lshl_add_u32 v6, s2, 7, v0
	v_cmp_gt_u32_e32 vcc, s0, v0
	s_waitcnt vmcnt(0)
	ds_write_b32 v1, v125
	s_and_saveexec_b64 s[4:5], vcc
	s_cbranch_execz .LBB2_6
	s_mov_b32 s0, 0xc350
	v_mov_b32_e32 v2, 0
	v_cmp_gt_i32_e64 s[0:1], s0, v6
	ds_write2st64_b32 v1, v2, v2 offset0:4 offset1:7
	ds_write_b32 v1, v2 offset:2560
	s_and_saveexec_b64 s[8:9], s[0:1]
	s_cbranch_execz .LBB2_5
	v_ashrrev_i32_e32 v7, 31, v6
	v_lshl_add_u64 v[2:3], v[6:7], 3, s[58:59]
	v_mov_b32_e32 v2, v124

	.amdhsa_kernel _Z5k_csrPKjS0_PK15HIP_vector_typeIiLj2EEPKiPiPjPS1_IfLj2EE
		.amdhsa_group_segment_fixed_size 4128
		.amdhsa_private_segment_fixed_size 0
		.amdhsa_kernarg_size 56
		.amdhsa_user_sgpr_count 2
		.amdhsa_user_sgpr_dispatch_ptr 0
		.amdhsa_user_sgpr_queue_ptr 0
		.amdhsa_user_sgpr_kernarg_segment_ptr 1
		.amdhsa_user_sgpr_dispatch_id 0
		.amdhsa_user_sgpr_kernarg_preload_length 0
		.amdhsa_user_sgpr_kernarg_preload_offset 0
		.amdhsa_user_sgpr_private_segment_size 0
		.amdhsa_uses_dynamic_stack 0
		.amdhsa_enable_private_segment 0
		.amdhsa_system_sgpr_workgroup_id_x 1
		.amdhsa_system_sgpr_workgroup_id_y 0
		.amdhsa_system_sgpr_workgroup_id_z 0
		.amdhsa_system_sgpr_workgroup_info 0
		.amdhsa_system_vgpr_workitem_id 0
		.amdhsa_next_free_vgpr 126
		.amdhsa_next_free_sgpr 68
		.amdhsa_accum_offset 128
		.amdhsa_reserve_vcc 1
		.amdhsa_float_round_mode_32 0
		.amdhsa_float_round_mode_16_64 0
		.amdhsa_float_denorm_mode_32 3
		.amdhsa_float_denorm_mode_16_64 3
		.amdhsa_dx10_clamp 1
		.amdhsa_ieee_mode 1
		.amdhsa_fp16_overflow 0
		.amdhsa_tg_split 0
		.amdhsa_exception_fp_ieee_invalid_op 0
		.amdhsa_exception_fp_denorm_src 0
		.amdhsa_exception_fp_ieee_div_zero 0
		.amdhsa_exception_fp_ieee_overflow 0
		.amdhsa_exception_fp_ieee_underflow 0
		.amdhsa_exception_fp_ieee_inexact 0
		.amdhsa_exception_int_div_zero 0
	.end_amdhsa_kernel

.LBB3_67:
	v_and_b32_e32 v114, 7, v19
	v_and_b32_e32 v115, 15, v0
	v_lshl_or_b32 v114, v114, 5, v115
	v_lshlrev_b32_e32 v114, 2, v114
	global_load_dword v112, v114, s[72:73]
	global_load_dword v113, v114, s[72:73] offset:64
	v_and_b32_e32 v105, 7, v19
	v_mov_b32_e32 v2, 0
	v_lshlrev_b32_e32 v4, 14, v105
	v_mov_b32_e32 v5, v2
	v_lshl_add_u64 v[4:5], s[22:23], 0, v[4:5]
	v_lshlrev_b32_e32 v6, 4, v18
	v_mov_b32_e32 v7, v2
	v_lshl_add_u64 v[98:99], v[4:5], 0, v[6:7]
	v_add_co_u32_e32 v4, vcc, 0x2000, v98
	global_load_dwordx4 v[26:29], v[98:99], off
	s_nop 0
	v_addc_co_u32_e32 v5, vcc, 0, v99, vcc
	global_load_dwordx4 v[30:33], v[4:5], off
	v_lshrrev_b32_e32 v103, 2, v0
	s_mov_b64 s[0:1], 0x2000
	v_and_b32_e32 v106, 15, v0
	v_and_b32_e32 v104, 0x80, v103
	v_and_b32_e32 v3, 48, v0
	s_movk_i32 s4, 0x210
	v_or_b32_e32 v4, v104, v106
	v_lshl_add_u64 v[100:101], v[98:99], 0, s[0:1]
	global_load_dwordx4 v[34:37], v[98:99], off offset:1024
	global_load_dwordx4 v[38:41], v[100:101], off offset:1024
	global_load_dwordx4 v[42:45], v[98:99], off offset:2048
	global_load_dwordx4 v[46:49], v[100:101], off offset:2048
	v_mad_u32_u24 v107, v4, s4, v3
	s_waitcnt lgkmcnt(0)
	s_barrier
	ds_read_b128 v[4:7], v107
	ds_read_b128 v[8:11], v107 offset:8448
	ds_read_b128 v[12:15], v107 offset:16896
	ds_read_b128 v[74:77], v107 offset:25344
	ds_read_b128 v[78:81], v107 offset:33792
	ds_read_b128 v[108:111], v107 offset:42240
	global_load_dwordx4 v[18:21], v[98:99], off offset:3072
	global_load_dwordx4 v[22:25], v[100:101], off offset:3072
	s_mov_b32 s8, 0
	s_mov_b32 s9, s8
	s_mov_b32 s10, s8
	s_mov_b32 s11, s8
	s_movk_i32 s0, 0x200
	v_cmp_gt_u32_e64 s[4:5], s0, v0
	s_waitcnt vmcnt(7) lgkmcnt(5)
	v_mfma_f32_16x16x32_f16 v[58:61], v[4:7], v[26:29], 0
	s_waitcnt lgkmcnt(4)
	v_mfma_f32_16x16x32_f16 v[66:69], v[8:11], v[26:29], 0
	s_waitcnt lgkmcnt(3)
	v_mfma_f32_16x16x32_f16 v[62:65], v[12:15], v[26:29], 0
	s_waitcnt lgkmcnt(2)
	v_mfma_f32_16x16x32_f16 v[70:73], v[74:77], v[26:29], 0
	s_waitcnt lgkmcnt(1)
	v_mfma_f32_16x16x32_f16 v[54:57], v[78:81], v[26:29], 0
	s_waitcnt lgkmcnt(0)
	v_mfma_f32_16x16x32_f16 v[50:53], v[108:111], v[26:29], 0
	s_waitcnt vmcnt(6)
	v_mfma_f32_16x16x32_f16 v[82:85], v[4:7], v[30:33], 0
	v_mfma_f32_16x16x32_f16 v[86:89], v[8:11], v[30:33], 0
	v_mov_b64_e32 v[6:7], s[8:9]
	v_mov_b64_e32 v[8:9], s[10:11]
	v_mfma_f32_16x16x32_f16 v[90:93], v[12:15], v[30:33], 0
	v_mov_b64_e32 v[16:17], s[10:11]
	v_mov_b64_e32 v[14:15], s[8:9]
	v_mfma_f32_16x16x32_f16 v[94:97], v[74:77], v[30:33], 0
	v_mfma_f32_16x16x32_f16 v[78:81], v[78:81], v[30:33], 0
	v_mfma_f32_16x16x32_f16 v[74:77], v[108:111], v[30:33], 0
	s_and_saveexec_b64 s[0:1], s[4:5]
	s_cbranch_execz .LBB3_69
	ds_read_b128 v[4:7], v107 offset:50688
	s_waitcnt lgkmcnt(0)
	v_mfma_f32_16x16x32_f16 v[14:17], v[4:7], v[26:29], 0
	v_mfma_f32_16x16x32_f16 v[6:9], v[4:7], v[30:33], 0

.LBB3_99:
	s_or_b64 exec, exec, s[0:1]
	v_lshl_or_b32 v56, v105, 5, v106
	v_lshlrev_b32_e32 v54, 2, v56
	v_and_b32_e32 v57, 0x8c, v103
	v_mov_b32_e32 v58, 0x22200
	v_lshl_add_u32 v58, v57, 2, v58
	ds_read_b128 v[74:77], v58 offset:0
	ds_read_b128 v[78:81], v58 offset:64
	ds_read_b128 v[82:85], v58 offset:128
	ds_read_b128 v[86:89], v58 offset:192
	ds_read_b128 v[90:93], v58 offset:256
	ds_read_b128 v[94:97], v58 offset:320
	v_sub_u32_e32 v98, s3, v57
	v_mov_b32_e32 v99, 0
	v_add_u32_e32 v107, 0, v98
	v_med3_i32 v107, v107, 0, 4
	v_add_u32_e32 v99, v99, v107
	v_add_u32_e32 v107, -16, v98
	v_med3_i32 v107, v107, 0, 4
	v_add_u32_e32 v99, v99, v107
	v_add_u32_e32 v107, -32, v98
	v_med3_i32 v107, v107, 0, 4
	v_add_u32_e32 v99, v99, v107
	v_add_u32_e32 v107, -48, v98
	v_med3_i32 v107, v107, 0, 4
	v_add_u32_e32 v99, v99, v107
	v_add_u32_e32 v107, -64, v98
	v_med3_i32 v107, v107, 0, 4
	v_add_u32_e32 v99, v99, v107
	v_add_u32_e32 v107, -80, v98
	v_med3_i32 v107, v107, 0, 4
	v_add_u32_e32 v99, v99, v107
	v_mov_b32_e32 v100, 0
	v_mov_b32_e32 v101, 0
	v_mov_b32_e32 v55, 24
	s_waitcnt vmcnt(0)
	s_waitcnt lgkmcnt(5)
	v_fma_f32 v108, v66, v74, v112
	v_fma_f32 v109, v30, v74, v113
	v_max_f32_e32 v108, 0, v108
	v_max_f32_e32 v109, 0, v109
	v_add_f32_e32 v100, v100, v108
	v_add_f32_e32 v101, v101, v109
	v_fma_f32 v108, v67, v75, v112
	v_fma_f32 v109, v31, v75, v113
	v_max_f32_e32 v108, 0, v108
	v_max_f32_e32 v109, 0, v109
	v_add_f32_e32 v100, v100, v108
	v_add_f32_e32 v101, v101, v109
	v_fma_f32 v108, v68, v76, v112
	v_fma_f32 v109, v32, v76, v113
	v_max_f32_e32 v108, 0, v108
	v_max_f32_e32 v109, 0, v109
	v_add_f32_e32 v100, v100, v108
	v_add_f32_e32 v101, v101, v109
	v_fma_f32 v108, v69, v77, v112
	v_fma_f32 v109, v33, v77, v113
	v_max_f32_e32 v108, 0, v108
	v_max_f32_e32 v109, 0, v109
	v_add_f32_e32 v100, v100, v108
	v_add_f32_e32 v101, v101, v109
	s_waitcnt lgkmcnt(4)
	v_fma_f32 v108, v62, v78, v112
	v_fma_f32 v109, v22, v78, v113
	v_max_f32_e32 v108, 0, v108
	v_max_f32_e32 v109, 0, v109
	v_add_f32_e32 v100, v100, v108
	v_add_f32_e32 v101, v101, v109
	v_fma_f32 v108, v63, v79, v112
	v_fma_f32 v109, v23, v79, v113
	v_max_f32_e32 v108, 0, v108
	v_max_f32_e32 v109, 0, v109
	v_add_f32_e32 v100, v100, v108
	v_add_f32_e32 v101, v101, v109
	v_fma_f32 v108, v64, v80, v112
	v_fma_f32 v109, v24, v80, v113
	v_max_f32_e32 v108, 0, v108
	v_max_f32_e32 v109, 0, v109
	v_add_f32_e32 v100, v100, v108
	v_add_f32_e32 v101, v101, v109
	v_fma_f32 v108, v65, v81, v112
	v_fma_f32 v109, v25, v81, v113
	v_max_f32_e32 v108, 0, v108
	v_max_f32_e32 v109, 0, v109
	v_add_f32_e32 v100, v100, v108
	v_add_f32_e32 v101, v101, v109
	s_waitcnt lgkmcnt(3)
	v_fma_f32 v108, v70, v82, v112
	v_fma_f32 v109, v34, v82, v113
	v_max_f32_e32 v108, 0, v108
	v_max_f32_e32 v109, 0, v109
	v_add_f32_e32 v100, v100, v108
	v_add_f32_e32 v101, v101, v109
	v_fma_f32 v108, v71, v83, v112
	v_fma_f32 v109, v35, v83, v113
	v_max_f32_e32 v108, 0, v108
	v_max_f32_e32 v109, 0, v109
	v_add_f32_e32 v100, v100, v108
	v_add_f32_e32 v101, v101, v109
	v_fma_f32 v108, v72, v84, v112
	v_fma_f32 v109, v36, v84, v113
	v_max_f32_e32 v108, 0, v108
	v_max_f32_e32 v109, 0, v109
	v_add_f32_e32 v100, v100, v108
	v_add_f32_e32 v101, v101, v109
	v_fma_f32 v108, v73, v85, v112
	v_fma_f32 v109, v37, v85, v113
	v_max_f32_e32 v108, 0, v108
	v_max_f32_e32 v109, 0, v109
	v_add_f32_e32 v100, v100, v108
	v_add_f32_e32 v101, v101, v109
	s_waitcnt lgkmcnt(2)
	v_fma_f32 v108, v50, v86, v112
	v_fma_f32 v109, v26, v86, v113
	v_max_f32_e32 v108, 0, v108
	v_max_f32_e32 v109, 0, v109
	v_add_f32_e32 v100, v100, v108
	v_add_f32_e32 v101, v101, v109
	v_fma_f32 v108, v51, v87, v112
	v_fma_f32 v109, v27, v87, v113
	v_max_f32_e32 v108, 0, v108
	v_max_f32_e32 v109, 0, v109
	v_add_f32_e32 v100, v100, v108
	v_add_f32_e32 v101, v101, v109
	v_fma_f32 v108, v52, v88, v112
	v_fma_f32 v109, v28, v88, v113
	v_max_f32_e32 v108, 0, v108
	v_max_f32_e32 v109, 0, v109
	v_add_f32_e32 v100, v100, v108
	v_add_f32_e32 v101, v101, v109
	v_fma_f32 v108, v53, v89, v112
	v_fma_f32 v109, v29, v89, v113
	v_max_f32_e32 v108, 0, v108
	v_max_f32_e32 v109, 0, v109
	v_add_f32_e32 v100, v100, v108
	v_add_f32_e32 v101, v101, v109
	s_waitcnt lgkmcnt(1)
	v_fma_f32 v108, v46, v90, v112
	v_fma_f32 v109, v38, v90, v113
	v_max_f32_e32 v108, 0, v108
	v_max_f32_e32 v109, 0, v109
	v_add_f32_e32 v100, v100, v108
	v_add_f32_e32 v101, v101, v109
	v_fma_f32 v108, v47, v91, v112
	v_fma_f32 v109, v39, v91, v113
	v_max_f32_e32 v108, 0, v108
	v_max_f32_e32 v109, 0, v109
	v_add_f32_e32 v100, v100, v108
	v_add_f32_e32 v101, v101, v109
	v_fma_f32 v108, v48, v92, v112
	v_fma_f32 v109, v40, v92, v113
	v_max_f32_e32 v108, 0, v108
	v_max_f32_e32 v109, 0, v109
	v_add_f32_e32 v100, v100, v108
	v_add_f32_e32 v101, v101, v109
	v_fma_f32 v108, v49, v93, v112
	v_fma_f32 v109, v41, v93, v113
	v_max_f32_e32 v108, 0, v108
	v_max_f32_e32 v109, 0, v109
	v_add_f32_e32 v100, v100, v108
	v_add_f32_e32 v101, v101, v109
	s_waitcnt lgkmcnt(0)
	v_fma_f32 v108, v42, v94, v112
	v_fma_f32 v109, v18, v94, v113
	v_max_f32_e32 v108, 0, v108
	v_max_f32_e32 v109, 0, v109
	v_add_f32_e32 v100, v100, v108
	v_add_f32_e32 v101, v101, v109
	v_fma_f32 v108, v43, v95, v112
	v_fma_f32 v109, v19, v95, v113
	v_max_f32_e32 v108, 0, v108
	v_max_f32_e32 v109, 0, v109
	v_add_f32_e32 v100, v100, v108
	v_add_f32_e32 v101, v101, v109
	v_fma_f32 v108, v44, v96, v112
	v_fma_f32 v109, v20, v96, v113
	v_max_f32_e32 v108, 0, v108
	v_max_f32_e32 v109, 0, v109
	v_add_f32_e32 v100, v100, v108
	v_add_f32_e32 v101, v101, v109
	v_fma_f32 v108, v45, v97, v112
	v_fma_f32 v109, v21, v97, v113
	v_max_f32_e32 v108, 0, v108
	v_max_f32_e32 v109, 0, v109
	v_add_f32_e32 v100, v100, v108
	v_add_f32_e32 v101, v101, v109
	s_and_b64 vcc, exec, s[4:5]
	s_cbranch_vccz .Lepi_tail
	ds_read_b128 v[74:77], v58 offset:384
	ds_read_b128 v[78:81], v58 offset:448
	v_add_u32_e32 v107, -96, v98
	v_med3_i32 v107, v107, 0, 4
	v_add_u32_e32 v99, v99, v107
	v_add_u32_e32 v107, -112, v98
	v_med3_i32 v107, v107, 0, 4
	v_add_u32_e32 v99, v99, v107
	v_mov_b32_e32 v55, 32
	s_waitcnt lgkmcnt(1)
	v_fma_f32 v108, v14, v74, v112
	v_fma_f32 v109, v6, v74, v113
	v_max_f32_e32 v108, 0, v108
	v_max_f32_e32 v109, 0, v109
	v_add_f32_e32 v100, v100, v108
	v_add_f32_e32 v101, v101, v109
	v_fma_f32 v108, v15, v75, v112
	v_fma_f32 v109, v7, v75, v113
	v_max_f32_e32 v108, 0, v108
	v_max_f32_e32 v109, 0, v109
	v_add_f32_e32 v100, v100, v108
	v_add_f32_e32 v101, v101, v109
	v_fma_f32 v108, v16, v76, v112
	v_fma_f32 v109, v8, v76, v113
	v_max_f32_e32 v108, 0, v108
	v_max_f32_e32 v109, 0, v109
	v_add_f32_e32 v100, v100, v108
	v_add_f32_e32 v101, v101, v109
	v_fma_f32 v108, v17, v77, v112
	v_fma_f32 v109, v9, v77, v113
	v_max_f32_e32 v108, 0, v108
	v_max_f32_e32 v109, 0, v109
	v_add_f32_e32 v100, v100, v108
	v_add_f32_e32 v101, v101, v109
	s_waitcnt lgkmcnt(0)
	v_fma_f32 v108, v10, v78, v112
	v_fma_f32 v109, v2, v78, v113
	v_max_f32_e32 v108, 0, v108
	v_max_f32_e32 v109, 0, v109
	v_add_f32_e32 v100, v100, v108
	v_add_f32_e32 v101, v101, v109
	v_fma_f32 v108, v11, v79, v112
	v_fma_f32 v109, v3, v79, v113
	v_max_f32_e32 v108, 0, v108
	v_max_f32_e32 v109, 0, v109
	v_add_f32_e32 v100, v100, v108
	v_add_f32_e32 v101, v101, v109
	v_fma_f32 v108, v12, v80, v112
	v_fma_f32 v109, v4, v80, v113
	v_max_f32_e32 v108, 0, v108
	v_max_f32_e32 v109, 0, v109
	v_add_f32_e32 v100, v100, v108
	v_add_f32_e32 v101, v101, v109
	v_fma_f32 v108, v13, v81, v112
	v_fma_f32 v109, v5, v81, v113
	v_max_f32_e32 v108, 0, v108
	v_max_f32_e32 v109, 0, v109
	v_add_f32_e32 v100, v100, v108
	v_add_f32_e32 v101, v101, v109
.Lepi_tail:
	v_sub_u32_e32 v99, v55, v99
	v_cvt_f32_i32_e32 v99, v99
	v_max_f32_e32 v108, 0, v112
	v_max_f32_e32 v109, 0, v113
	v_fma_f32 v100, -v99, v108, v100
	v_fma_f32 v101, -v99, v109, v101
	ds_bpermute_b32 v2, v102, v100
	ds_bpermute_b32 v3, v102, v101
	v_mov_b32_e32 v4, 0x21e00
	v_lshl_add_u32 v4, v56, 2, v4
	s_waitcnt lgkmcnt(0)
	v_add_f32_e32 v100, v100, v2
	v_add_f32_e32 v101, v101, v3
	ds_bpermute_b32 v2, v1, v100
	ds_bpermute_b32 v3, v1, v101
	s_waitcnt lgkmcnt(0)
	v_add_f32_e32 v100, v100, v2
	v_add_f32_e32 v101, v101, v3
	s_and_saveexec_b64 s[0:1], s[66:67]
	ds_add_f32 v4, v100
	ds_add_f32 v4, v101 offset:64

_Z7k_finalPKfS0_S0_S0_S0_S0_S0_S0_S0_S0_Pf:
	s_load_dwordx8 s[4:11], s[0:1], 0x0
	s_load_dwordx8 s[12:19], s[0:1], 0x20
	s_load_dwordx4 s[20:23], s[0:1], 0x40
	s_load_dwordx2 s[24:25], s[0:1], 0x50
	v_lshlrev_b32_e32 v1, 2, v0
	v_and_b32_e32 v2, 15, v0
	v_lshrrev_b32_e32 v3, 4, v0
	s_lshl_b32 s3, s2, 6
	v_cmp_gt_u32_e32 vcc, 64, v0
	s_waitcnt lgkmcnt(0)
	s_load_dwordx16 s[32:47], s[6:7], 0x0
	s_and_saveexec_b64 s[26:27], vcc
	s_cbranch_execz .Lkf_nomlp
	global_load_dword v100, v1, s[10:11]
	global_load_dword v101, v1, s[8:9] offset:0
	global_load_dword v102, v1, s[8:9] offset:256
	global_load_dword v103, v1, s[8:9] offset:512
	global_load_dword v104, v1, s[8:9] offset:768
	global_load_dword v105, v1, s[8:9] offset:1024
	global_load_dword v106, v1, s[8:9] offset:1280
	global_load_dword v107, v1, s[8:9] offset:1536
	global_load_dword v108, v1, s[8:9] offset:1792
	global_load_dword v109, v1, s[8:9] offset:2048
	global_load_dword v110, v1, s[8:9] offset:2304
	global_load_dword v111, v1, s[8:9] offset:2560
	global_load_dword v112, v1, s[8:9] offset:2816
	global_load_dword v113, v1, s[8:9] offset:3072
	global_load_dword v114, v1, s[8:9] offset:3328
	global_load_dword v115, v1, s[8:9] offset:3584
	global_load_dword v116, v1, s[8:9] offset:3840
	global_load_dword v117, v1, s[14:15]
	global_load_dword v118, v1, s[12:13] offset:0
	global_load_dword v119, v1, s[12:13] offset:256
	global_load_dword v120, v1, s[12:13] offset:512
	global_load_dword v121, v1, s[12:13] offset:768
	global_load_dword v122, v1, s[12:13] offset:1024
	global_load_dword v123, v1, s[12:13] offset:1280
	global_load_dword v124, v1, s[12:13] offset:1536
	global_load_dword v125, v1, s[12:13] offset:1792
	global_load_dword v126, v1, s[12:13] offset:2048
	global_load_dword v127, v1, s[12:13] offset:2304
	global_load_dword v128, v1, s[12:13] offset:2560
	global_load_dword v129, v1, s[12:13] offset:2816
	global_load_dword v130, v1, s[12:13] offset:3072
	global_load_dword v131, v1, s[12:13] offset:3328
	global_load_dword v132, v1, s[12:13] offset:3584
	global_load_dword v133, v1, s[12:13] offset:3840
	s_add_u32 s28, s12, 0x1000
	s_addc_u32 s29, s13, 0
	global_load_dword v134, v1, s[28:29] offset:0
	global_load_dword v135, v1, s[28:29] offset:256
	global_load_dword v136, v1, s[28:29] offset:512
	global_load_dword v137, v1, s[28:29] offset:768
	global_load_dword v138, v1, s[28:29] offset:1024
	global_load_dword v139, v1, s[28:29] offset:1280
	global_load_dword v140, v1, s[28:29] offset:1536
	global_load_dword v141, v1, s[28:29] offset:1792
	global_load_dword v142, v1, s[28:29] offset:2048
	global_load_dword v143, v1, s[28:29] offset:2304
	global_load_dword v144, v1, s[28:29] offset:2560
	global_load_dword v145, v1, s[28:29] offset:2816
	global_load_dword v146, v1, s[28:29] offset:3072
	global_load_dword v147, v1, s[28:29] offset:3328
	global_load_dword v148, v1, s[28:29] offset:3584
	global_load_dword v149, v1, s[28:29] offset:3840
	s_add_u32 s28, s12, 0x2000
	s_addc_u32 s29, s13, 0
	global_load_dword v150, v1, s[28:29] offset:0
	global_load_dword v151, v1, s[28:29] offset:256
	global_load_dword v152, v1, s[28:29] offset:512
	global_load_dword v153, v1, s[28:29] offset:768
	global_load_dword v154, v1, s[28:29] offset:1024
	global_load_dword v155, v1, s[28:29] offset:1280
	global_load_dword v156, v1, s[28:29] offset:1536
	global_load_dword v157, v1, s[28:29] offset:1792
	global_load_dword v158, v1, s[28:29] offset:2048
	global_load_dword v159, v1, s[28:29] offset:2304
	global_load_dword v160, v1, s[28:29] offset:2560
	global_load_dword v161, v1, s[28:29] offset:2816
	global_load_dword v162, v1, s[28:29] offset:3072
	global_load_dword v163, v1, s[28:29] offset:3328
	global_load_dword v164, v1, s[28:29] offset:3584
	global_load_dword v165, v1, s[28:29] offset:3840
	s_add_u32 s28, s12, 0x3000
	s_addc_u32 s29, s13, 0
	global_load_dword v166, v1, s[28:29] offset:0
	global_load_dword v167, v1, s[28:29] offset:256
	global_load_dword v168, v1, s[28:29] offset:512
	global_load_dword v169, v1, s[28:29] offset:768
	global_load_dword v170, v1, s[28:29] offset:1024
	global_load_dword v171, v1, s[28:29] offset:1280
	global_load_dword v172, v1, s[28:29] offset:1536
	global_load_dword v173, v1, s[28:29] offset:1792
	global_load_dword v174, v1, s[28:29] offset:2048
	global_load_dword v175, v1, s[28:29] offset:2304
	global_load_dword v176, v1, s[28:29] offset:2560
	global_load_dword v177, v1, s[28:29] offset:2816
	global_load_dword v178, v1, s[28:29] offset:3072
	global_load_dword v179, v1, s[28:29] offset:3328
	global_load_dword v180, v1, s[28:29] offset:3584
	global_load_dword v181, v1, s[28:29] offset:3840
	v_cmp_gt_u32_e32 vcc, 16, v0
	s_and_saveexec_b64 s[30:31], vcc
	v_add_u32_e32 v7, s3, v1
	global_load_dword v94, v7, s[18:19]
	v_cmp_gt_u32_e32 vcc, 4, v0
	s_and_b64 exec, exec, vcc
	s_lshl_b32 s28, s3, 2
	v_add_u32_e32 v8, s28, v1
	global_load_dword v95, v1, s[22:23]
	global_load_dword v182, v8, s[20:21] offset:0
	global_load_dword v183, v8, s[20:21] offset:16
	global_load_dword v184, v8, s[20:21] offset:32
	global_load_dword v185, v8, s[20:21] offset:48
	global_load_dword v186, v8, s[20:21] offset:64
	global_load_dword v187, v8, s[20:21] offset:80
	global_load_dword v188, v8, s[20:21] offset:96
	global_load_dword v189, v8, s[20:21] offset:112
	global_load_dword v190, v8, s[20:21] offset:128
	global_load_dword v191, v8, s[20:21] offset:144
	global_load_dword v192, v8, s[20:21] offset:160
	global_load_dword v193, v8, s[20:21] offset:176
	global_load_dword v194, v8, s[20:21] offset:192
	global_load_dword v195, v8, s[20:21] offset:208
	global_load_dword v196, v8, s[20:21] offset:224
	global_load_dword v197, v8, s[20:21] offset:240
.Lkf_nomlp:
	s_mov_b64 exec, -1
	v_mul_u32_u24_e32 v4, 0x5000, v3
	v_lshl_add_u32 v4, v2, 2, v4
	v_add_u32_e32 v4, s3, v4
	global_load_dword v10, v4, s[16:17] offset:0
	global_load_dword v11, v4, s[16:17] offset:1024
	global_load_dword v12, v4, s[16:17] offset:2048
	global_load_dword v13, v4, s[16:17] offset:3072
	v_add_u32_e32 v4, 0x1000, v4
	global_load_dword v14, v4, s[16:17] offset:0
	global_load_dword v15, v4, s[16:17] offset:1024
	global_load_dword v16, v4, s[16:17] offset:2048
	global_load_dword v17, v4, s[16:17] offset:3072
	v_add_u32_e32 v4, 0x1000, v4
	global_load_dword v18, v4, s[16:17] offset:0
	global_load_dword v19, v4, s[16:17] offset:1024
	global_load_dword v20, v4, s[16:17] offset:2048
	global_load_dword v21, v4, s[16:17] offset:3072
	v_add_u32_e32 v4, 0x1000, v4
	global_load_dword v22, v4, s[16:17] offset:0
	global_load_dword v23, v4, s[16:17] offset:1024
	global_load_dword v24, v4, s[16:17] offset:2048
	global_load_dword v25, v4, s[16:17] offset:3072
	v_add_u32_e32 v4, 0x1000, v4
	global_load_dword v26, v4, s[16:17] offset:0
	global_load_dword v27, v4, s[16:17] offset:1024
	global_load_dword v28, v4, s[16:17] offset:2048
	global_load_dword v29, v4, s[16:17] offset:3072
	v_mov_b32_e32 v6, v1
	global_load_dword v30, v6, s[4:5] offset:0
	global_load_dword v31, v6, s[4:5] offset:1024
	global_load_dword v32, v6, s[4:5] offset:2048
	global_load_dword v33, v6, s[4:5] offset:3072
	v_add_u32_e32 v6, 0x1000, v6
	global_load_dword v34, v6, s[4:5] offset:0
	global_load_dword v35, v6, s[4:5] offset:1024
	global_load_dword v36, v6, s[4:5] offset:2048
	global_load_dword v37, v6, s[4:5] offset:3072
	v_add_u32_e32 v6, 0x1000, v6
	global_load_dword v38, v6, s[4:5] offset:0
	global_load_dword v39, v6, s[4:5] offset:1024
	global_load_dword v40, v6, s[4:5] offset:2048
	global_load_dword v41, v6, s[4:5] offset:3072
	v_add_u32_e32 v6, 0x1000, v6
	global_load_dword v42, v6, s[4:5] offset:0
	global_load_dword v43, v6, s[4:5] offset:1024
	global_load_dword v44, v6, s[4:5] offset:2048
	global_load_dword v45, v6, s[4:5] offset:3072
	v_add_u32_e32 v6, 0x1000, v6
	global_load_dword v46, v6, s[4:5] offset:0
	global_load_dword v47, v6, s[4:5] offset:1024
	global_load_dword v48, v6, s[4:5] offset:2048
	global_load_dword v49, v6, s[4:5] offset:3072
	v_add_u32_e32 v6, 0x1000, v6
	global_load_dword v50, v6, s[4:5] offset:0
	global_load_dword v51, v6, s[4:5] offset:1024
	global_load_dword v52, v6, s[4:5] offset:2048
	global_load_dword v53, v6, s[4:5] offset:3072
	v_add_u32_e32 v6, 0x1000, v6
	global_load_dword v54, v6, s[4:5] offset:0
	global_load_dword v55, v6, s[4:5] offset:1024
	global_load_dword v56, v6, s[4:5] offset:2048
	global_load_dword v57, v6, s[4:5] offset:3072
	v_add_u32_e32 v6, 0x1000, v6
	global_load_dword v58, v6, s[4:5] offset:0
	global_load_dword v59, v6, s[4:5] offset:1024
	global_load_dword v60, v6, s[4:5] offset:2048
	global_load_dword v61, v6, s[4:5] offset:3072
	v_add_u32_e32 v6, 0x1000, v6
	global_load_dword v62, v6, s[4:5] offset:0
	global_load_dword v63, v6, s[4:5] offset:1024
	global_load_dword v64, v6, s[4:5] offset:2048
	global_load_dword v65, v6, s[4:5] offset:3072
	v_add_u32_e32 v6, 0x1000, v6
	global_load_dword v66, v6, s[4:5] offset:0
	global_load_dword v67, v6, s[4:5] offset:1024
	global_load_dword v68, v6, s[4:5] offset:2048
	global_load_dword v69, v6, s[4:5] offset:3072
	v_add_u32_e32 v6, 0x1000, v6
	global_load_dword v70, v6, s[4:5] offset:0
	global_load_dword v71, v6, s[4:5] offset:1024
	global_load_dword v72, v6, s[4:5] offset:2048
	global_load_dword v73, v6, s[4:5] offset:3072
	v_add_u32_e32 v6, 0x1000, v6
	global_load_dword v74, v6, s[4:5] offset:0
	global_load_dword v75, v6, s[4:5] offset:1024
	global_load_dword v76, v6, s[4:5] offset:2048
	global_load_dword v77, v6, s[4:5] offset:3072
	v_add_u32_e32 v6, 0x1000, v6
	global_load_dword v78, v6, s[4:5] offset:0
	global_load_dword v79, v6, s[4:5] offset:1024
	global_load_dword v80, v6, s[4:5] offset:2048
	global_load_dword v81, v6, s[4:5] offset:3072
	v_add_u32_e32 v6, 0x1000, v6
	global_load_dword v82, v6, s[4:5] offset:0
	global_load_dword v83, v6, s[4:5] offset:1024
	global_load_dword v84, v6, s[4:5] offset:2048
	global_load_dword v85, v6, s[4:5] offset:3072
	v_add_u32_e32 v6, 0x1000, v6
	global_load_dword v86, v6, s[4:5] offset:0
	global_load_dword v87, v6, s[4:5] offset:1024
	global_load_dword v88, v6, s[4:5] offset:2048
	global_load_dword v89, v6, s[4:5] offset:3072
	v_add_u32_e32 v6, 0x1000, v6
	global_load_dword v90, v6, s[4:5] offset:0
	global_load_dword v91, v6, s[4:5] offset:1024
	global_load_dword v92, v6, s[4:5] offset:2048
	global_load_dword v93, v6, s[4:5] offset:3072
	v_mov_b32_e32 v9, 0
	v_cmp_gt_u32_e32 vcc, 64, v0
	s_and_saveexec_b64 s[26:27], vcc
	s_cbranch_execz .Lkf_mlpdone
	s_waitcnt vmcnt(63) lgkmcnt(0)
	v_mov_b32_e32 v96, v100
	v_fmac_f32_e32 v96, s32, v101
	v_fmac_f32_e32 v96, s33, v102
	v_fmac_f32_e32 v96, s34, v103
	v_fmac_f32_e32 v96, s35, v104
	v_fmac_f32_e32 v96, s36, v105
	v_fmac_f32_e32 v96, s37, v106
	v_fmac_f32_e32 v96, s38, v107
	v_fmac_f32_e32 v96, s39, v108
	v_fmac_f32_e32 v96, s40, v109
	v_fmac_f32_e32 v96, s41, v110
	v_fmac_f32_e32 v96, s42, v111
	v_fmac_f32_e32 v96, s43, v112
	v_fmac_f32_e32 v96, s44, v113
	v_fmac_f32_e32 v96, s45, v114
	v_fmac_f32_e32 v96, s46, v115
	v_fmac_f32_e32 v96, s47, v116
	v_max_f32_e32 v96, 0, v96
	ds_write_b32 v1, v96 offset:1280
	v_mov_b32_e32 v97, v117
	s_waitcnt lgkmcnt(0)
	ds_read_b128 v[200:203], v9 offset:1280
	ds_read_b128 v[204:207], v9 offset:1296
	ds_read_b128 v[208:211], v9 offset:1312
	ds_read_b128 v[212:215], v9 offset:1328
	s_waitcnt lgkmcnt(3)
	v_fmac_f32_e32 v97, v200, v118
	v_fmac_f32_e32 v97, v201, v119
	v_fmac_f32_e32 v97, v202, v120
	v_fmac_f32_e32 v97, v203, v121
	s_waitcnt lgkmcnt(2)
	v_fmac_f32_e32 v97, v204, v122
	v_fmac_f32_e32 v97, v205, v123
	v_fmac_f32_e32 v97, v206, v124
	v_fmac_f32_e32 v97, v207, v125
	s_waitcnt lgkmcnt(1)
	v_fmac_f32_e32 v97, v208, v126
	v_fmac_f32_e32 v97, v209, v127
	v_fmac_f32_e32 v97, v210, v128
	v_fmac_f32_e32 v97, v211, v129
	s_waitcnt lgkmcnt(0)
	v_fmac_f32_e32 v97, v212, v130
	v_fmac_f32_e32 v97, v213, v131
	v_fmac_f32_e32 v97, v214, v132
	v_fmac_f32_e32 v97, v215, v133
	ds_read_b128 v[200:203], v9 offset:1344
	ds_read_b128 v[204:207], v9 offset:1360
	ds_read_b128 v[208:211], v9 offset:1376
	ds_read_b128 v[212:215], v9 offset:1392
	s_waitcnt lgkmcnt(3)
	v_fmac_f32_e32 v97, v200, v134
	v_fmac_f32_e32 v97, v201, v135
	v_fmac_f32_e32 v97, v202, v136
	v_fmac_f32_e32 v97, v203, v137
	s_waitcnt lgkmcnt(2)
	v_fmac_f32_e32 v97, v204, v138
	v_fmac_f32_e32 v97, v205, v139
	v_fmac_f32_e32 v97, v206, v140
	v_fmac_f32_e32 v97, v207, v141
	s_waitcnt lgkmcnt(1)
	v_fmac_f32_e32 v97, v208, v142
	v_fmac_f32_e32 v97, v209, v143
	v_fmac_f32_e32 v97, v210, v144
	v_fmac_f32_e32 v97, v211, v145
	s_waitcnt lgkmcnt(0)
	v_fmac_f32_e32 v97, v212, v146
	v_fmac_f32_e32 v97, v213, v147
	v_fmac_f32_e32 v97, v214, v148
	v_fmac_f32_e32 v97, v215, v149
	ds_read_b128 v[200:203], v9 offset:1408
	ds_read_b128 v[204:207], v9 offset:1424
	ds_read_b128 v[208:211], v9 offset:1440
	ds_read_b128 v[212:215], v9 offset:1456
	s_waitcnt lgkmcnt(3)
	v_fmac_f32_e32 v97, v200, v150
	v_fmac_f32_e32 v97, v201, v151
	v_fmac_f32_e32 v97, v202, v152
	v_fmac_f32_e32 v97, v203, v153
	s_waitcnt lgkmcnt(2)
	v_fmac_f32_e32 v97, v204, v154
	v_fmac_f32_e32 v97, v205, v155
	v_fmac_f32_e32 v97, v206, v156
	v_fmac_f32_e32 v97, v207, v157
	s_waitcnt lgkmcnt(1)
	v_fmac_f32_e32 v97, v208, v158
	v_fmac_f32_e32 v97, v209, v159
	v_fmac_f32_e32 v97, v210, v160
	v_fmac_f32_e32 v97, v211, v161
	s_waitcnt lgkmcnt(0)
	v_fmac_f32_e32 v97, v212, v162
	v_fmac_f32_e32 v97, v213, v163
	v_fmac_f32_e32 v97, v214, v164
	v_fmac_f32_e32 v97, v215, v165
	ds_read_b128 v[200:203], v9 offset:1472
	ds_read_b128 v[204:207], v9 offset:1488
	ds_read_b128 v[208:211], v9 offset:1504
	ds_read_b128 v[212:215], v9 offset:1520
	s_waitcnt lgkmcnt(3)
	v_fmac_f32_e32 v97, v200, v166
	v_fmac_f32_e32 v97, v201, v167
	v_fmac_f32_e32 v97, v202, v168
	v_fmac_f32_e32 v97, v203, v169
	s_waitcnt lgkmcnt(2)
	v_fmac_f32_e32 v97, v204, v170
	v_fmac_f32_e32 v97, v205, v171
	v_fmac_f32_e32 v97, v206, v172
	v_fmac_f32_e32 v97, v207, v173
	s_waitcnt lgkmcnt(1)
	v_fmac_f32_e32 v97, v208, v174
	v_fmac_f32_e32 v97, v209, v175
	v_fmac_f32_e32 v97, v210, v176
	v_fmac_f32_e32 v97, v211, v177
	s_waitcnt lgkmcnt(0)
	v_fmac_f32_e32 v97, v212, v178
	v_fmac_f32_e32 v97, v213, v179
	v_fmac_f32_e32 v97, v214, v180
	v_fmac_f32_e32 v97, v215, v181
	ds_write_b32 v1, v97 offset:1024
	s_cmp_lg_u32 s2, 0
	s_cbranch_scc1 .Lkf_mlpdone
	global_store_dword v1, v97, s[24:25] offset:1024
.Lkf_mlpdone:
	s_mov_b64 exec, -1
	s_waitcnt vmcnt(0)
	v_add_f32_e32 v200, v30, v34
	v_add_f32_e32 v201, v31, v35
	v_add_f32_e32 v202, v32, v36
	v_add_f32_e32 v203, v33, v37
	v_add_f32_e32 v200, v200, v38
	v_add_f32_e32 v201, v201, v39
	v_add_f32_e32 v202, v202, v40
	v_add_f32_e32 v203, v203, v41
	v_add_f32_e32 v200, v200, v42
	v_add_f32_e32 v201, v201, v43
	v_add_f32_e32 v202, v202, v44
	v_add_f32_e32 v203, v203, v45
	v_add_f32_e32 v200, v200, v46
	v_add_f32_e32 v201, v201, v47
	v_add_f32_e32 v202, v202, v48
	v_add_f32_e32 v203, v203, v49
	v_add_f32_e32 v200, v200, v50
	v_add_f32_e32 v201, v201, v51
	v_add_f32_e32 v202, v202, v52
	v_add_f32_e32 v203, v203, v53
	v_add_f32_e32 v200, v200, v54
	v_add_f32_e32 v201, v201, v55
	v_add_f32_e32 v202, v202, v56
	v_add_f32_e32 v203, v203, v57
	v_add_f32_e32 v200, v200, v58
	v_add_f32_e32 v201, v201, v59
	v_add_f32_e32 v202, v202, v60
	v_add_f32_e32 v203, v203, v61
	v_add_f32_e32 v200, v200, v62
	v_add_f32_e32 v201, v201, v63
	v_add_f32_e32 v202, v202, v64
	v_add_f32_e32 v203, v203, v65
	v_add_f32_e32 v200, v200, v66
	v_add_f32_e32 v201, v201, v67
	v_add_f32_e32 v202, v202, v68
	v_add_f32_e32 v203, v203, v69
	v_add_f32_e32 v200, v200, v70
	v_add_f32_e32 v201, v201, v71
	v_add_f32_e32 v202, v202, v72
	v_add_f32_e32 v203, v203, v73
	v_add_f32_e32 v200, v200, v74
	v_add_f32_e32 v201, v201, v75
	v_add_f32_e32 v202, v202, v76
	v_add_f32_e32 v203, v203, v77
	v_add_f32_e32 v200, v200, v78
	v_add_f32_e32 v201, v201, v79
	v_add_f32_e32 v202, v202, v80
	v_add_f32_e32 v203, v203, v81
	v_add_f32_e32 v200, v200, v82
	v_add_f32_e32 v201, v201, v83
	v_add_f32_e32 v202, v202, v84
	v_add_f32_e32 v203, v203, v85
	v_add_f32_e32 v200, v200, v86
	v_add_f32_e32 v201, v201, v87
	v_add_f32_e32 v202, v202, v88
	v_add_f32_e32 v203, v203, v89
	v_add_f32_e32 v200, v200, v90
	v_add_f32_e32 v201, v201, v91
	v_add_f32_e32 v202, v202, v92
	v_add_f32_e32 v203, v203, v93
	v_add_f32_e32 v200, v200, v201
	v_add_f32_e32 v202, v202, v203
	v_add_f32_e32 v98, v200, v202
	ds_write_b32 v1, v98
	s_cmp_lg_u32 s2, 0
	s_cbranch_scc1 .Lkf_nog
	global_store_dword v1, v98, s[24:25]
.Lkf_nog:
	s_waitcnt lgkmcnt(0)
	s_barrier
	v_mul_u32_u24_e32 v5, 0x50, v3
	ds_read_b128 v[200:203], v5 offset:0
	ds_read_b128 v[204:207], v5 offset:16
	ds_read_b128 v[208:211], v5 offset:32
	ds_read_b128 v[212:215], v5 offset:48
	ds_read_b128 v[216:219], v5 offset:64
	v_mov_b32_e32 v99, 0
	s_waitcnt lgkmcnt(4)
	v_fmac_f32_e32 v99, v200, v10
	v_fmac_f32_e32 v99, v201, v11
	v_fmac_f32_e32 v99, v202, v12
	v_fmac_f32_e32 v99, v203, v13
	s_waitcnt lgkmcnt(3)
	v_fmac_f32_e32 v99, v204, v14
	v_fmac_f32_e32 v99, v205, v15
	v_fmac_f32_e32 v99, v206, v16
	v_fmac_f32_e32 v99, v207, v17
	s_waitcnt lgkmcnt(2)
	v_fmac_f32_e32 v99, v208, v18
	v_fmac_f32_e32 v99, v209, v19
	v_fmac_f32_e32 v99, v210, v20
	v_fmac_f32_e32 v99, v211, v21
	s_waitcnt lgkmcnt(1)
	v_fmac_f32_e32 v99, v212, v22
	v_fmac_f32_e32 v99, v213, v23
	v_fmac_f32_e32 v99, v214, v24
	v_fmac_f32_e32 v99, v215, v25
	s_waitcnt lgkmcnt(0)
	v_fmac_f32_e32 v99, v216, v26
	v_fmac_f32_e32 v99, v217, v27
	v_fmac_f32_e32 v99, v218, v28
	v_fmac_f32_e32 v99, v219, v29
	v_mad_u32_u24 v6, v3, 17, v2
	v_lshlrev_b32_e32 v6, 2, v6
	ds_write_b32 v6, v99 offset:1536
	s_waitcnt lgkmcnt(0)
	s_barrier
	v_cmp_gt_u32_e32 vcc, 16, v0
	s_and_saveexec_b64 s[26:27], vcc
	s_cbranch_execz .Lkf_end
	ds_read_b32 v220, v1 offset:1536
	ds_read_b32 v221, v1 offset:1604
	ds_read_b32 v222, v1 offset:1672
	ds_read_b32 v223, v1 offset:1740
	ds_read_b32 v224, v1 offset:1808
	ds_read_b32 v225, v1 offset:1876
	ds_read_b32 v226, v1 offset:1944
	ds_read_b32 v227, v1 offset:2012
	ds_read_b32 v228, v1 offset:2080
	ds_read_b32 v229, v1 offset:2148
	ds_read_b32 v230, v1 offset:2216
	ds_read_b32 v231, v1 offset:2284
	ds_read_b32 v232, v1 offset:2352
	ds_read_b32 v233, v1 offset:2420
	ds_read_b32 v234, v1 offset:2488
	ds_read_b32 v235, v1 offset:2556
	s_waitcnt lgkmcnt(0)
	v_add_f32_e32 v94, v94, v220
	v_add_f32_e32 v94, v94, v221
	v_add_f32_e32 v94, v94, v222
	v_add_f32_e32 v94, v94, v223
	v_add_f32_e32 v94, v94, v224
	v_add_f32_e32 v94, v94, v225
	v_add_f32_e32 v94, v94, v226
	v_add_f32_e32 v94, v94, v227
	v_add_f32_e32 v94, v94, v228
	v_add_f32_e32 v94, v94, v229
	v_add_f32_e32 v94, v94, v230
	v_add_f32_e32 v94, v94, v231
	v_add_f32_e32 v94, v94, v232
	v_add_f32_e32 v94, v94, v233
	v_add_f32_e32 v94, v94, v234
	v_add_f32_e32 v94, v94, v235
	v_max_f32_e32 v94, 0, v94
	ds_write_b32 v1, v94 offset:2624
	v_cmp_gt_u32_e32 vcc, 4, v0
	s_waitcnt lgkmcnt(0)
	s_and_b64 exec, exec, vcc
	s_cbranch_execz .Lkf_end
	ds_read_b128 v[240:243], v9 offset:2624
	ds_read_b128 v[244:247], v9 offset:2640
	ds_read_b128 v[248:251], v9 offset:2656
	ds_read_b128 v[252:255], v9 offset:2672
	s_cmp_eq_u32 s2, 0
	s_cselect_b64 vcc, -1, 0
	s_nop 1
	v_cndmask_b32_e32 v95, 0, v95, vcc
	s_waitcnt lgkmcnt(0)
	v_fmac_f32_e32 v95, v240, v182
	v_fmac_f32_e32 v95, v241, v183
	v_fmac_f32_e32 v95, v242, v184
	v_fmac_f32_e32 v95, v243, v185
	v_fmac_f32_e32 v95, v244, v186
	v_fmac_f32_e32 v95, v245, v187
	v_fmac_f32_e32 v95, v246, v188
	v_fmac_f32_e32 v95, v247, v189
	v_fmac_f32_e32 v95, v248, v190
	v_fmac_f32_e32 v95, v249, v191
	v_fmac_f32_e32 v95, v250, v192
	v_fmac_f32_e32 v95, v251, v193
	v_fmac_f32_e32 v95, v252, v194
	v_fmac_f32_e32 v95, v253, v195
	v_fmac_f32_e32 v95, v254, v196
	v_fmac_f32_e32 v95, v255, v197
	global_atomic_add_f32 v1, v95, s[24:25] offset:1280

	.amdhsa_kernel _Z7k_finalPKfS0_S0_S0_S0_S0_S0_S0_S0_S0_Pf
		.amdhsa_group_segment_fixed_size 2688
		.amdhsa_private_segment_fixed_size 0
		.amdhsa_kernarg_size 88
		.amdhsa_user_sgpr_count 2
		.amdhsa_user_sgpr_dispatch_ptr 0
		.amdhsa_user_sgpr_queue_ptr 0
		.amdhsa_user_sgpr_kernarg_segment_ptr 1
		.amdhsa_user_sgpr_dispatch_id 0
		.amdhsa_user_sgpr_kernarg_preload_length 0
		.amdhsa_user_sgpr_kernarg_preload_offset 0
		.amdhsa_user_sgpr_private_segment_size 0
		.amdhsa_uses_dynamic_stack 0
		.amdhsa_enable_private_segment 0
		.amdhsa_system_sgpr_workgroup_id_x 1
		.amdhsa_system_sgpr_workgroup_id_y 0
		.amdhsa_system_sgpr_workgroup_id_z 0
		.amdhsa_system_sgpr_workgroup_info 0
		.amdhsa_system_vgpr_workitem_id 0
		.amdhsa_next_free_vgpr 256
		.amdhsa_next_free_sgpr 48
		.amdhsa_accum_offset 256
		.amdhsa_reserve_vcc 1
		.amdhsa_float_round_mode_32 0
		.amdhsa_float_round_mode_16_64 0
		.amdhsa_float_denorm_mode_32 3
		.amdhsa_float_denorm_mode_16_64 3
		.amdhsa_dx10_clamp 1
		.amdhsa_ieee_mode 1
		.amdhsa_fp16_overflow 0
		.amdhsa_tg_split 0
		.amdhsa_exception_fp_ieee_invalid_op 0
		.amdhsa_exception_fp_denorm_src 0
		.amdhsa_exception_fp_ieee_div_zero 0
		.amdhsa_exception_fp_ieee_overflow 0
		.amdhsa_exception_fp_ieee_underflow 0
		.amdhsa_exception_fp_ieee_inexact 0
		.amdhsa_exception_int_div_zero 0
	.end_amdhsa_kernel

amdhsa.kernels:
  - .agpr_count:     0
    .args:
      - .actual_access:  read_only
        .address_space:  global
        .offset:         0
        .size:           8
        .value_kind:     global_buffer
      - .actual_access:  read_only
        .address_space:  global
        .offset:         8
        .size:           8
        .value_kind:     global_buffer
      - .actual_access:  write_only
        .address_space:  global
        .offset:         16
        .size:           8
        .value_kind:     global_buffer
      - .actual_access:  write_only
        .address_space:  global
        .offset:         24
        .size:           8
        .value_kind:     global_buffer
      - .actual_access:  write_only
        .address_space:  global
        .offset:         32
        .size:           8
        .value_kind:     global_buffer
      - .actual_access:  write_only
        .address_space:  global
        .offset:         40
        .size:           8
        .value_kind:     global_buffer
      - .actual_access:  write_only
        .address_space:  global
        .offset:         48
        .size:           8
        .value_kind:     global_buffer
      - .actual_access:  write_only
        .address_space:  global
        .offset:         56
        .size:           8
        .value_kind:     global_buffer
      - .actual_access:  read_only
        .address_space:  global
        .offset:         64
        .size:           8
        .value_kind:     global_buffer
      - .actual_access:  write_only
        .address_space:  global
        .offset:         72
        .size:           8
        .value_kind:     global_buffer
    .group_segment_fixed_size: 18800
    .kernarg_segment_align: 8
    .kernarg_segment_size: 80
    .language:       OpenCL C
    .language_version:
      - 2
      - 0
    .max_flat_workgroup_size: 1024
    .name:           _Z6k_partPKiS0_PjPhS1_S1_PfS3_PKfPDF16_
    .private_segment_fixed_size: 0
    .sgpr_count:     48
    .sgpr_spill_count: 0
    .symbol:         _Z6k_partPKiS0_PjPhS1_S1_PfS3_PKfPDF16_.kd
    .uniform_work_group_size: 1
    .uses_dynamic_stack: false
    .vgpr_count:     40
    .vgpr_spill_count: 0
    .wavefront_size: 64
  - .agpr_count:     0
    .args:
      - .actual_access:  read_only
        .address_space:  global
        .offset:         0
        .size:           8
        .value_kind:     global_buffer
      - .actual_access:  read_only
        .address_space:  global
        .offset:         8
        .size:           8
        .value_kind:     global_buffer
      - .actual_access:  read_only
        .address_space:  global
        .offset:         16
        .size:           8
        .value_kind:     global_buffer
      - .actual_access:  read_only
        .address_space:  global
        .offset:         24
        .size:           8
        .value_kind:     global_buffer
      - .actual_access:  write_only
        .address_space:  global
        .offset:         32
        .size:           8
        .value_kind:     global_buffer
      - .actual_access:  write_only
        .address_space:  global
        .offset:         40
        .size:           8
        .value_kind:     global_buffer
    .group_segment_fixed_size: 3076
    .kernarg_segment_align: 8
    .kernarg_segment_size: 48
    .language:       OpenCL C
    .language_version:
      - 2
      - 0
    .max_flat_workgroup_size: 512
    .name:           _Z5k_degPKjPKhS0_S0_P15HIP_vector_typeIiLj2EEPi
    .private_segment_fixed_size: 0
    .sgpr_count:     74
    .sgpr_spill_count: 0
    .symbol:         _Z5k_degPKjPKhS0_S0_P15HIP_vector_typeIiLj2EEPi.kd
    .uniform_work_group_size: 1
    .uses_dynamic_stack: false
    .vgpr_count:     61
    .vgpr_spill_count: 0
    .wavefront_size: 64
  - .agpr_count:     0
    .args:
      - .actual_access:  read_only
        .address_space:  global
        .offset:         0
        .size:           8
        .value_kind:     global_buffer
      - .actual_access:  read_only
        .address_space:  global
        .offset:         8
        .size:           8
        .value_kind:     global_buffer
      - .actual_access:  read_only
        .address_space:  global
        .offset:         16
        .size:           8
        .value_kind:     global_buffer
      - .actual_access:  read_only
        .address_space:  global
        .offset:         24
        .size:           8
        .value_kind:     global_buffer
      - .actual_access:  write_only
        .address_space:  global
        .offset:         32
        .size:           8
        .value_kind:     global_buffer
      - .actual_access:  write_only
        .address_space:  global
        .offset:         40
        .size:           8
        .value_kind:     global_buffer
      - .actual_access:  write_only
        .address_space:  global
        .offset:         48
        .size:           8
        .value_kind:     global_buffer
    .group_segment_fixed_size: 4128
    .kernarg_segment_align: 8
    .kernarg_segment_size: 56
    .language:       OpenCL C
    .language_version:
      - 2
      - 0
    .max_flat_workgroup_size: 256
    .name:           _Z5k_csrPKjS0_PK15HIP_vector_typeIiLj2EEPKiPiPjPS1_IfLj2EE
    .private_segment_fixed_size: 0
    .sgpr_count:     74
    .sgpr_spill_count: 0
    .symbol:         _Z5k_csrPKjS0_PK15HIP_vector_typeIiLj2EEPKiPiPjPS1_IfLj2EE.kd
    .uniform_work_group_size: 1
    .uses_dynamic_stack: false
    .vgpr_count:     126
    .vgpr_spill_count: 0
    .wavefront_size: 64
  - .agpr_count:     0
    .args:
      - .actual_access:  read_only
        .address_space:  global
        .offset:         0
        .size:           8
        .value_kind:     global_buffer
      - .actual_access:  read_only
        .address_space:  global
        .offset:         8
        .size:           8
        .value_kind:     global_buffer
      - .actual_access:  read_only
        .address_space:  global
        .offset:         16
        .size:           8
        .value_kind:     global_buffer
      - .actual_access:  read_only
        .address_space:  global
        .offset:         24
        .size:           8
        .value_kind:     global_buffer
      - .actual_access:  read_only
        .address_space:  global
        .offset:         32
        .size:           8
        .value_kind:     global_buffer
      - .actual_access:  read_only
        .address_space:  global
        .offset:         40
        .size:           8
        .value_kind:     global_buffer
      - .actual_access:  read_only
        .address_space:  global
        .offset:         48
        .size:           8
        .value_kind:     global_buffer
      - .address_space:  global
        .offset:         56
        .size:           8
        .value_kind:     global_buffer
    .group_segment_fixed_size: 151664
    .kernarg_segment_align: 8
    .kernarg_segment_size: 64
    .language:       OpenCL C
    .language_version:
      - 2
      - 0
    .max_flat_workgroup_size: 1024
    .name:           _Z6k_mainPKiPKjPK15HIP_vector_typeIfLj2EEPKfS8_PKDF16_S8_Pf
    .private_segment_fixed_size: 0
    .sgpr_count:     84
    .sgpr_spill_count: 0
    .symbol:         _Z6k_mainPKiPKjPK15HIP_vector_typeIfLj2EEPKfS8_PKDF16_S8_Pf.kd
    .uniform_work_group_size: 1
    .uses_dynamic_stack: false
    .vgpr_count:     128
    .vgpr_spill_count: 0
    .wavefront_size: 64
  - .agpr_count:     0
    .args:
      - .actual_access:  read_only
        .address_space:  global
        .offset:         0
        .size:           8
        .value_kind:     global_buffer
      - .actual_access:  read_only
        .address_space:  global
        .offset:         8
        .size:           8
        .value_kind:     global_buffer
      - .actual_access:  read_only
        .address_space:  global
        .offset:         16
        .size:           8
        .value_kind:     global_buffer
      - .actual_access:  read_only
        .address_space:  global
        .offset:         24
        .size:           8
        .value_kind:     global_buffer
      - .actual_access:  read_only
        .address_space:  global
        .offset:         32
        .size:           8
        .value_kind:     global_buffer
      - .actual_access:  read_only
        .address_space:  global
        .offset:         40
        .size:           8
        .value_kind:     global_buffer
      - .actual_access:  read_only
        .address_space:  global
        .offset:         48
        .size:           8
        .value_kind:     global_buffer
      - .actual_access:  read_only
        .address_space:  global
        .offset:         56
        .size:           8
        .value_kind:     global_buffer
      - .actual_access:  read_only
        .address_space:  global
        .offset:         64
        .size:           8
        .value_kind:     global_buffer
      - .actual_access:  read_only
        .address_space:  global
        .offset:         72
        .size:           8
        .value_kind:     global_buffer
      - .address_space:  global
        .offset:         80
        .size:           8
        .value_kind:     global_buffer
    .group_segment_fixed_size: 2688
    .kernarg_segment_align: 8
    .kernarg_segment_size: 88
    .language:       OpenCL C
    .language_version:
      - 2
      - 0
    .max_flat_workgroup_size: 256
    .name:           _Z7k_finalPKfS0_S0_S0_S0_S0_S0_S0_S0_S0_Pf
    .private_segment_fixed_size: 0
    .sgpr_count:     54
    .sgpr_spill_count: 0
    .symbol:         _Z7k_finalPKfS0_S0_S0_S0_S0_S0_S0_S0_S0_Pf.kd
    .uniform_work_group_size: 1
    .uses_dynamic_stack: false
    .vgpr_count:     256
    .vgpr_spill_count: 0
    .wavefront_size: 64
